# speedup vs baseline: 1.0041x; 1.0041x over previous
.LBB2_355:
	s_or_b64 exec, exec, s[52:53]
	s_add_u32 s52, s92, 0x80
	s_addc_u32 s53, s93, 0
	s_add_i32 s82, 0, 0x18000
	s_add_i32 s58, s82, s57
	s_waitcnt vmcnt(8)
	v_mfma_f32_16x16x32_f16 v[102:105], v[30:33], v[6:9], 0
	s_mov_b32 m0, s58
	s_waitcnt vmcnt(4)
	v_lshl_add_u32 v248, v149, 4, v152
	v_lshlrev_b32_e32 v248, 2, v248
	v_add_u32_e32 v248, 0x20000, v248
	ds_write_b32 v248, v246
	ds_write_b32 v248, v247 offset:512
	s_barrier
	v_mfma_f32_16x16x32_f16 v[98:101], v[26:29], v[6:9], 0
	v_mfma_f32_16x16x32_f16 v[126:129], v[30:33], v[2:5], 0
	v_mfma_f32_16x16x32_f16 v[122:125], v[26:29], v[2:5], 0
	v_mfma_f32_16x16x32_f16 v[118:121], v[30:33], v[14:17], 0
	v_mfma_f32_16x16x32_f16 v[110:113], v[30:33], v[10:13], 0
	v_mfma_f32_16x16x32_f16 v[94:97], v[142:145], v[6:9], 0
	v_mfma_f32_16x16x32_f16 v[90:93], v[138:141], v[6:9], 0
	v_mfma_f32_16x16x32_f16 v[86:89], v[142:145], v[2:5], 0
	v_mfma_f32_16x16x32_f16 v[82:85], v[138:141], v[2:5], 0
	v_mfma_f32_16x16x32_f16 v[62:65], v[30:33], v[22:25], 0
	v_mfma_f32_16x16x32_f16 v[54:57], v[30:33], v[18:21], 0
	v_mfma_f32_16x16x32_f16 v[46:49], v[30:33], v[134:137], 0
	v_mfma_f32_16x16x32_f16 v[38:41], v[30:33], v[130:133], 0
	v_mfma_f32_16x16x32_f16 v[30:33], v[26:29], v[130:133], 0
	v_mfma_f32_16x16x32_f16 v[6:9], v[142:145], v[130:133], 0
	v_mfma_f32_16x16x32_f16 v[2:5], v[138:141], v[130:133], 0
	v_lshl_add_u64 v[130:131], s[52:53], 0, v[162:163]
	s_add_u32 s52, s52, 0x20000
	global_load_lds_dwordx4 v[130:131], off
	s_addc_u32 s53, s53, 0
	s_add_i32 m0, s58, 0x2000
	s_add_u32 s58, s90, 0x80
	s_addc_u32 s59, s91, 0
	v_lshl_add_u64 v[130:131], s[52:53], 0, v[162:163]
	s_add_i32 s52, s97, 0x8000
	global_load_lds_dwordx4 v[130:131], off
	v_lshl_add_u64 v[130:131], s[58:59], 0, v[162:163]
	s_add_u32 s58, s58, 0x20000
	s_addc_u32 s59, s59, 0
	s_mov_b32 m0, s52
	s_add_i32 s53, s97, 0xa000
	global_load_lds_dwordx4 v[130:131], off
	v_lshl_add_u64 v[130:131], s[58:59], 0, v[162:163]
	s_add_u32 s58, s92, 0x40080
	s_addc_u32 s59, s93, 0
	s_add_i32 s83, 0, 0x1c000
	s_mov_b32 m0, s53
	s_add_i32 s57, s83, s57
	global_load_lds_dwordx4 v[130:131], off
	v_lshl_add_u64 v[130:131], s[58:59], 0, v[162:163]
	s_add_u32 s58, s58, 0x20000
	s_mov_b32 m0, s57
	s_addc_u32 s59, s59, 0
	global_load_lds_dwordx4 v[130:131], off
	s_add_i32 m0, s57, 0x2000
	v_lshl_add_u64 v[130:131], s[58:59], 0, v[162:163]
	global_load_lds_dwordx4 v[130:131], off
	v_lshlrev_b32_e32 v132, 2, v152
	v_lshlrev_b32_e32 v130, 6, v152
	v_and_b32_e32 v131, 32, v132
	v_bitop3_b32 v130, v130, v131, v146 bitop3:0x36
	s_add_i32 s57, 0, 0x10000
	v_add_u32_e32 v131, s57, v130
	s_add_i32 s57, 0, 0x14000
	v_mfma_f32_16x16x32_f16 v[114:117], v[26:29], v[14:17], 0
	s_waitcnt vmcnt(6)
	v_lshlrev_b32_e32 v133, 13, v154
	s_barrier
	v_mfma_f32_16x16x32_f16 v[106:109], v[26:29], v[10:13], 0
	v_mfma_f32_16x16x32_f16 v[78:81], v[142:145], v[14:17], 0
	v_mfma_f32_16x16x32_f16 v[74:77], v[138:141], v[14:17], 0
	v_mfma_f32_16x16x32_f16 v[70:73], v[142:145], v[10:13], 0
	v_mfma_f32_16x16x32_f16 v[66:69], v[138:141], v[10:13], 0
	v_mfma_f32_16x16x32_f16 v[58:61], v[26:29], v[22:25], 0
	v_mfma_f32_16x16x32_f16 v[50:53], v[26:29], v[18:21], 0
	v_mfma_f32_16x16x32_f16 v[42:45], v[26:29], v[134:137], 0
	v_mfma_f32_16x16x32_f16 v[34:37], v[142:145], v[22:25], 0
	v_mfma_f32_16x16x32_f16 v[26:29], v[138:141], v[22:25], 0
	v_mfma_f32_16x16x32_f16 v[22:25], v[142:145], v[18:21], 0
	v_mfma_f32_16x16x32_f16 v[18:21], v[138:141], v[18:21], 0
	v_mfma_f32_16x16x32_f16 v[14:17], v[142:145], v[134:137], 0
	v_mfma_f32_16x16x32_f16 v[10:13], v[138:141], v[134:137], 0
	v_add_u32_e32 v136, s57, v130
	v_add_u32_e32 v139, s82, v130
	v_add_u32_e32 v140, s83, v130
	v_or_b32_e32 v130, v151, v152
	v_lshlrev_b32_e32 v134, 6, v130
	s_movk_i32 s57, 0x3c0
	v_lshlrev_b32_e32 v130, 2, v130
	v_and_or_b32 v134, v134, s57, v146
	v_and_b32_e32 v130, 32, v130
	v_xad_u32 v130, v134, v130, 0
	v_or_b32_e32 v134, 16, v151
	v_or_b32_e32 v137, v134, v152
	v_lshlrev_b32_e32 v138, 6, v137
	v_lshlrev_b32_e32 v137, 2, v137
	v_and_or_b32 v138, v138, s57, v146
	v_and_b32_e32 v137, 32, v137
	v_lshlrev_b32_e32 v141, 7, v134
	v_or_b32_e32 v134, 32, v151
	v_xad_u32 v137, v138, v137, 0
	v_or_b32_e32 v138, v134, v152
	v_lshlrev_b32_e32 v142, 6, v138
	v_lshlrev_b32_e32 v138, 2, v138
	v_and_or_b32 v142, v142, s57, v146
	v_and_b32_e32 v138, 32, v138
	v_lshlrev_b32_e32 v143, 7, v134
	v_or_b32_e32 v134, 48, v151
	v_xad_u32 v142, v142, v138, 0
	v_or_b32_e32 v138, v134, v152
	v_lshlrev_b32_e32 v144, 6, v138
	v_lshlrev_b32_e32 v138, 2, v138
	v_and_or_b32 v144, v144, s57, v146
	v_and_b32_e32 v138, 32, v138
	v_lshlrev_b32_e32 v135, 12, v153
	v_xad_u32 v144, v144, v138, 0
	v_lshlrev_b32_e32 v145, 7, v134
	s_mov_b32 s57, 0
	v_add_u32_e32 v138, v131, v135
	v_add_u32_e32 v134, v130, v133
	v_add_u32_e32 v133, v137, v141
	v_add_u32_e32 v131, v142, v143
	v_add_u32_e32 v130, v144, v145
	v_add_u32_e32 v137, v136, v135
	v_add_u32_e32 v136, v139, v135
	v_add_u32_e32 v135, v140, v135
	s_cmp_lg_u32 s100, 0
	s_cbranch_scc1 .Lg2p_loop
	s_branch .LBB2_356

.LBB2_356:
	ds_read_b128 v[140:143], v138
	ds_read_b128 v[154:157], v138 offset:1024
	ds_read_b128 v[158:161], v138 offset:2048
	ds_read_b128 v[164:167], v138 offset:3072
	s_lshl_b32 vcc_hi, s57, 7
	s_add_u32 s58, s88, vcc_hi
	s_addc_u32 s59, s89, 0
	s_add_u32 s82, s58, 0x80
	s_addc_u32 s83, s59, 0
	s_add_i32 s59, s97, 0xc000
	s_mov_b32 m0, s59
	s_add_i32 s58, s97, 0xe000
	ds_read_b128 v[168:171], v134
	ds_read_b128 v[172:175], v134 offset:1024
	ds_read_b128 v[176:179], v133
	ds_read_b128 v[184:187], v133 offset:1024
	ds_read_b128 v[188:191], v131
	ds_read_b128 v[192:195], v131 offset:1024
	ds_read_b128 v[196:199], v130
	ds_read_b128 v[200:203], v130 offset:1024
	global_load_lds_dwordx4 v162, s[82:83]
	s_mov_b32 m0, s58
	s_add_u32 s82, s82, 0x20000
	s_addc_u32 s83, s83, 0
	global_load_lds_dwordx4 v162, s[82:83]
	s_waitcnt lgkmcnt(8)
	s_barrier
	s_waitcnt lgkmcnt(0)
	v_mfma_f32_16x16x32_f16 v[102:105], v[140:143], v[168:171], v[102:105]
	v_mfma_f32_16x16x32_f16 v[98:101], v[158:161], v[168:171], v[98:101]
	v_mfma_f32_16x16x32_f16 v[126:129], v[140:143], v[176:179], v[126:129]
	v_mfma_f32_16x16x32_f16 v[122:125], v[158:161], v[176:179], v[122:125]
	v_mfma_f32_16x16x32_f16 v[118:121], v[140:143], v[188:191], v[118:121]
	v_mfma_f32_16x16x32_f16 v[114:117], v[158:161], v[188:191], v[114:117]
	v_mfma_f32_16x16x32_f16 v[110:113], v[140:143], v[196:199], v[110:113]
	v_mfma_f32_16x16x32_f16 v[106:109], v[158:161], v[196:199], v[106:109]
	v_mfma_f32_16x16x32_f16 v[102:105], v[154:157], v[172:175], v[102:105]
	v_mfma_f32_16x16x32_f16 v[98:101], v[164:167], v[172:175], v[98:101]
	v_mfma_f32_16x16x32_f16 v[126:129], v[154:157], v[184:187], v[126:129]
	v_mfma_f32_16x16x32_f16 v[122:125], v[164:167], v[184:187], v[122:125]
	v_mfma_f32_16x16x32_f16 v[118:121], v[154:157], v[192:195], v[118:121]
	v_mfma_f32_16x16x32_f16 v[114:117], v[164:167], v[192:195], v[114:117]
	v_mfma_f32_16x16x32_f16 v[110:113], v[154:157], v[200:203], v[110:113]
	v_mfma_f32_16x16x32_f16 v[106:109], v[164:167], v[200:203], v[106:109]
	s_barrier
	s_add_i32 vcc_lo, s57, 2
	s_lshl_b32 s78, vcc_lo, 7
	s_add_u32 s82, s92, s78
	s_addc_u32 s83, s93, 0
	s_mov_b32 m0, s84
	ds_read_b128 v[204:207], v137
	ds_read_b128 v[208:211], v137 offset:1024
	ds_read_b128 v[212:215], v137 offset:2048
	ds_read_b128 v[216:219], v137 offset:3072
	global_load_lds_dwordx4 v162, s[82:83]
	s_mov_b32 m0, s94
	s_add_u32 s82, s82, 0x20000
	s_addc_u32 s83, s83, 0
	global_load_lds_dwordx4 v162, s[82:83]
	s_barrier
	s_waitcnt lgkmcnt(0)
	v_mfma_f32_16x16x32_f16 v[94:97], v[204:207], v[168:171], v[94:97]
	v_mfma_f32_16x16x32_f16 v[90:93], v[212:215], v[168:171], v[90:93]
	v_mfma_f32_16x16x32_f16 v[86:89], v[204:207], v[176:179], v[86:89]
	v_mfma_f32_16x16x32_f16 v[82:85], v[212:215], v[176:179], v[82:85]
	v_mfma_f32_16x16x32_f16 v[78:81], v[204:207], v[188:191], v[78:81]
	v_mfma_f32_16x16x32_f16 v[74:77], v[212:215], v[188:191], v[74:77]
	v_mfma_f32_16x16x32_f16 v[70:73], v[204:207], v[196:199], v[70:73]
	v_mfma_f32_16x16x32_f16 v[66:69], v[212:215], v[196:199], v[66:69]
	v_mfma_f32_16x16x32_f16 v[94:97], v[208:211], v[172:175], v[94:97]
	v_mfma_f32_16x16x32_f16 v[90:93], v[216:219], v[172:175], v[90:93]
	v_mfma_f32_16x16x32_f16 v[86:89], v[208:211], v[184:187], v[86:89]
	v_mfma_f32_16x16x32_f16 v[82:85], v[216:219], v[184:187], v[82:85]
	v_mfma_f32_16x16x32_f16 v[78:81], v[208:211], v[192:195], v[78:81]
	v_mfma_f32_16x16x32_f16 v[74:77], v[216:219], v[192:195], v[74:77]
	v_mfma_f32_16x16x32_f16 v[70:73], v[208:211], v[200:203], v[70:73]
	v_mfma_f32_16x16x32_f16 v[66:69], v[216:219], v[200:203], v[66:69]
	s_add_u32 s82, s90, s78
	s_addc_u32 s83, s91, 0
	s_mov_b32 m0, s97
	s_barrier
	ds_read_b128 v[168:171], v134 offset:16384
	ds_read_b128 v[172:175], v134 offset:17408
	ds_read_b128 v[176:179], v133 offset:16384
	ds_read_b128 v[184:187], v133 offset:17408
	ds_read_b128 v[188:191], v131 offset:16384
	ds_read_b128 v[192:195], v131 offset:17408
	ds_read_b128 v[196:199], v130 offset:16384
	ds_read_b128 v[200:203], v130 offset:17408
	global_load_lds_dwordx4 v162, s[82:83]
	s_mov_b32 m0, s99
	s_add_u32 s82, s82, 0x20000
	s_addc_u32 s83, s83, 0
	global_load_lds_dwordx4 v162, s[82:83]
	s_barrier
	s_waitcnt lgkmcnt(0)
	v_mfma_f32_16x16x32_f16 v[62:65], v[140:143], v[168:171], v[62:65]
	v_mfma_f32_16x16x32_f16 v[58:61], v[158:161], v[168:171], v[58:61]
	v_mfma_f32_16x16x32_f16 v[54:57], v[140:143], v[176:179], v[54:57]
	v_mfma_f32_16x16x32_f16 v[50:53], v[158:161], v[176:179], v[50:53]
	v_mfma_f32_16x16x32_f16 v[46:49], v[140:143], v[188:191], v[46:49]
	v_mfma_f32_16x16x32_f16 v[42:45], v[158:161], v[188:191], v[42:45]
	v_mfma_f32_16x16x32_f16 v[38:41], v[140:143], v[196:199], v[38:41]
	v_mfma_f32_16x16x32_f16 v[30:33], v[158:161], v[196:199], v[30:33]
	v_mfma_f32_16x16x32_f16 v[62:65], v[154:157], v[172:175], v[62:65]
	v_mfma_f32_16x16x32_f16 v[58:61], v[164:167], v[172:175], v[58:61]
	v_mfma_f32_16x16x32_f16 v[54:57], v[154:157], v[184:187], v[54:57]
	v_mfma_f32_16x16x32_f16 v[50:53], v[164:167], v[184:187], v[50:53]
	v_mfma_f32_16x16x32_f16 v[46:49], v[154:157], v[192:195], v[46:49]
	v_mfma_f32_16x16x32_f16 v[42:45], v[164:167], v[192:195], v[42:45]
	v_mfma_f32_16x16x32_f16 v[38:41], v[154:157], v[200:203], v[38:41]
	v_mfma_f32_16x16x32_f16 v[30:33], v[164:167], v[200:203], v[30:33]
	s_barrier
	s_add_u32 s82, s34, s78
	s_addc_u32 s83, s35, 0
	s_mov_b32 m0, s95
	s_nop 0
	global_load_lds_dwordx4 v162, s[82:83]
	s_mov_b32 m0, s33
	s_add_u32 s82, s82, 0x20000
	s_addc_u32 s83, s83, 0
	global_load_lds_dwordx4 v162, s[82:83]
	s_waitcnt vmcnt(6)
	s_barrier
	v_mfma_f32_16x16x32_f16 v[34:37], v[204:207], v[168:171], v[34:37]
	v_mfma_f32_16x16x32_f16 v[26:29], v[212:215], v[168:171], v[26:29]
	v_mfma_f32_16x16x32_f16 v[22:25], v[204:207], v[176:179], v[22:25]
	v_mfma_f32_16x16x32_f16 v[18:21], v[212:215], v[176:179], v[18:21]
	v_mfma_f32_16x16x32_f16 v[14:17], v[204:207], v[188:191], v[14:17]
	v_mfma_f32_16x16x32_f16 v[10:13], v[212:215], v[188:191], v[10:13]
	v_mfma_f32_16x16x32_f16 v[6:9], v[204:207], v[196:199], v[6:9]
	v_mfma_f32_16x16x32_f16 v[2:5], v[212:215], v[196:199], v[2:5]
	v_mfma_f32_16x16x32_f16 v[34:37], v[208:211], v[172:175], v[34:37]
	v_mfma_f32_16x16x32_f16 v[26:29], v[216:219], v[172:175], v[26:29]
	v_mfma_f32_16x16x32_f16 v[22:25], v[208:211], v[184:187], v[22:25]
	v_mfma_f32_16x16x32_f16 v[18:21], v[216:219], v[184:187], v[18:21]
	v_mfma_f32_16x16x32_f16 v[14:17], v[208:211], v[192:195], v[14:17]
	v_mfma_f32_16x16x32_f16 v[10:13], v[216:219], v[192:195], v[10:13]
	v_mfma_f32_16x16x32_f16 v[6:9], v[208:211], v[200:203], v[6:9]
	v_mfma_f32_16x16x32_f16 v[2:5], v[216:219], v[200:203], v[2:5]
	s_barrier
	ds_read_b128 v[140:143], v136
	ds_read_b128 v[154:157], v136 offset:1024
	ds_read_b128 v[158:161], v136 offset:2048
	ds_read_b128 v[164:167], v136 offset:3072
	s_add_u32 s82, s88, s78
	s_addc_u32 s83, s89, 0
	s_mov_b32 m0, s11
	ds_read_b128 v[168:171], v134 offset:32768
	ds_read_b128 v[172:175], v134 offset:33792
	ds_read_b128 v[176:179], v133 offset:32768
	ds_read_b128 v[184:187], v133 offset:33792
	ds_read_b128 v[188:191], v131 offset:32768
	ds_read_b128 v[192:195], v131 offset:33792
	ds_read_b128 v[196:199], v130 offset:32768
	ds_read_b128 v[200:203], v130 offset:33792
	global_load_lds_dwordx4 v162, s[82:83]
	s_mov_b32 m0, s56
	s_add_u32 s82, s82, 0x20000
	s_addc_u32 s83, s83, 0
	global_load_lds_dwordx4 v162, s[82:83]
	s_waitcnt lgkmcnt(8)
	s_barrier
	s_waitcnt lgkmcnt(0)
	v_mfma_f32_16x16x32_f16 v[102:105], v[140:143], v[168:171], v[102:105]
	v_mfma_f32_16x16x32_f16 v[98:101], v[158:161], v[168:171], v[98:101]
	v_mfma_f32_16x16x32_f16 v[126:129], v[140:143], v[176:179], v[126:129]
	v_mfma_f32_16x16x32_f16 v[122:125], v[158:161], v[176:179], v[122:125]
	v_mfma_f32_16x16x32_f16 v[118:121], v[140:143], v[188:191], v[118:121]
	v_mfma_f32_16x16x32_f16 v[114:117], v[158:161], v[188:191], v[114:117]
	v_mfma_f32_16x16x32_f16 v[110:113], v[140:143], v[196:199], v[110:113]
	v_mfma_f32_16x16x32_f16 v[106:109], v[158:161], v[196:199], v[106:109]
	v_mfma_f32_16x16x32_f16 v[102:105], v[154:157], v[172:175], v[102:105]
	v_mfma_f32_16x16x32_f16 v[98:101], v[164:167], v[172:175], v[98:101]
	v_mfma_f32_16x16x32_f16 v[126:129], v[154:157], v[184:187], v[126:129]
	v_mfma_f32_16x16x32_f16 v[122:125], v[164:167], v[184:187], v[122:125]
	v_mfma_f32_16x16x32_f16 v[118:121], v[154:157], v[192:195], v[118:121]
	v_mfma_f32_16x16x32_f16 v[114:117], v[164:167], v[192:195], v[114:117]
	v_mfma_f32_16x16x32_f16 v[110:113], v[154:157], v[200:203], v[110:113]
	v_mfma_f32_16x16x32_f16 v[106:109], v[164:167], v[200:203], v[106:109]
	s_barrier
	s_add_u32 s78, s92, vcc_hi
	s_addc_u32 s79, s93, 0
	s_add_u32 s82, s78, 0x180
	s_addc_u32 s83, s79, 0
	s_add_i32 m0, s97, 0x18000
	ds_read_b128 v[204:207], v135
	ds_read_b128 v[208:211], v135 offset:1024
	ds_read_b128 v[212:215], v135 offset:2048
	ds_read_b128 v[216:219], v135 offset:3072
	global_load_lds_dwordx4 v162, s[82:83]
	s_add_i32 m0, s97, 0x1a000
	s_add_u32 s82, s82, 0x20000
	s_addc_u32 s83, s83, 0
	global_load_lds_dwordx4 v162, s[82:83]
	s_barrier
	s_waitcnt lgkmcnt(0)
	v_mfma_f32_16x16x32_f16 v[94:97], v[204:207], v[168:171], v[94:97]
	v_mfma_f32_16x16x32_f16 v[90:93], v[212:215], v[168:171], v[90:93]
	v_mfma_f32_16x16x32_f16 v[86:89], v[204:207], v[176:179], v[86:89]
	v_mfma_f32_16x16x32_f16 v[82:85], v[212:215], v[176:179], v[82:85]
	v_mfma_f32_16x16x32_f16 v[78:81], v[204:207], v[188:191], v[78:81]
	v_mfma_f32_16x16x32_f16 v[74:77], v[212:215], v[188:191], v[74:77]
	v_mfma_f32_16x16x32_f16 v[70:73], v[204:207], v[196:199], v[70:73]
	v_mfma_f32_16x16x32_f16 v[66:69], v[212:215], v[196:199], v[66:69]
	v_mfma_f32_16x16x32_f16 v[94:97], v[208:211], v[172:175], v[94:97]
	v_mfma_f32_16x16x32_f16 v[90:93], v[216:219], v[172:175], v[90:93]
	v_mfma_f32_16x16x32_f16 v[86:89], v[208:211], v[184:187], v[86:89]
	v_mfma_f32_16x16x32_f16 v[82:85], v[216:219], v[184:187], v[82:85]
	v_mfma_f32_16x16x32_f16 v[78:81], v[208:211], v[192:195], v[78:81]
	v_mfma_f32_16x16x32_f16 v[74:77], v[216:219], v[192:195], v[74:77]
	v_mfma_f32_16x16x32_f16 v[70:73], v[208:211], v[200:203], v[70:73]
	v_mfma_f32_16x16x32_f16 v[66:69], v[216:219], v[200:203], v[66:69]
	s_add_u32 s78, s90, vcc_hi
	s_addc_u32 s79, s91, 0
	s_add_u32 s82, s78, 0x180
	s_addc_u32 s83, s79, 0
	s_mov_b32 m0, s52
	s_barrier
	ds_read_b128 v[168:171], v134 offset:49152
	ds_read_b128 v[172:175], v134 offset:50176
	ds_read_b128 v[176:179], v133 offset:49152
	ds_read_b128 v[184:187], v133 offset:50176
	ds_read_b128 v[188:191], v131 offset:49152
	ds_read_b128 v[192:195], v131 offset:50176
	ds_read_b128 v[196:199], v130 offset:49152
	ds_read_b128 v[200:203], v130 offset:50176
	global_load_lds_dwordx4 v162, s[82:83]
	s_mov_b32 m0, s53
	s_add_u32 s82, s82, 0x20000
	s_addc_u32 s83, s83, 0
	global_load_lds_dwordx4 v162, s[82:83]
	s_barrier
	s_waitcnt lgkmcnt(0)
	v_mfma_f32_16x16x32_f16 v[62:65], v[140:143], v[168:171], v[62:65]
	v_mfma_f32_16x16x32_f16 v[58:61], v[158:161], v[168:171], v[58:61]
	v_mfma_f32_16x16x32_f16 v[54:57], v[140:143], v[176:179], v[54:57]
	v_mfma_f32_16x16x32_f16 v[50:53], v[158:161], v[176:179], v[50:53]
	v_mfma_f32_16x16x32_f16 v[46:49], v[140:143], v[188:191], v[46:49]
	v_mfma_f32_16x16x32_f16 v[42:45], v[158:161], v[188:191], v[42:45]
	v_mfma_f32_16x16x32_f16 v[38:41], v[140:143], v[196:199], v[38:41]
	v_mfma_f32_16x16x32_f16 v[30:33], v[158:161], v[196:199], v[30:33]
	v_mfma_f32_16x16x32_f16 v[62:65], v[154:157], v[172:175], v[62:65]
	v_mfma_f32_16x16x32_f16 v[58:61], v[164:167], v[172:175], v[58:61]
	v_mfma_f32_16x16x32_f16 v[54:57], v[154:157], v[184:187], v[54:57]
	v_mfma_f32_16x16x32_f16 v[50:53], v[164:167], v[184:187], v[50:53]
	v_mfma_f32_16x16x32_f16 v[46:49], v[154:157], v[192:195], v[46:49]
	v_mfma_f32_16x16x32_f16 v[42:45], v[164:167], v[192:195], v[42:45]
	v_mfma_f32_16x16x32_f16 v[38:41], v[154:157], v[200:203], v[38:41]
	v_mfma_f32_16x16x32_f16 v[30:33], v[164:167], v[200:203], v[30:33]
	s_barrier
	s_add_u32 s78, s34, vcc_hi
	s_addc_u32 s79, s35, 0
	s_add_u32 s82, s78, 0x180
	s_addc_u32 s83, s79, 0
	s_add_i32 m0, s97, 0x1c000
	s_nop 0
	global_load_lds_dwordx4 v162, s[82:83]
	s_add_i32 m0, s97, 0x1e000
	s_add_u32 s82, s82, 0x20000
	s_addc_u32 s83, s83, 0
	global_load_lds_dwordx4 v162, s[82:83]
	s_waitcnt vmcnt(6)
	s_barrier
	v_mfma_f32_16x16x32_f16 v[34:37], v[204:207], v[168:171], v[34:37]
	v_mfma_f32_16x16x32_f16 v[26:29], v[212:215], v[168:171], v[26:29]
	v_mfma_f32_16x16x32_f16 v[22:25], v[204:207], v[176:179], v[22:25]
	v_mfma_f32_16x16x32_f16 v[18:21], v[212:215], v[176:179], v[18:21]
	v_mfma_f32_16x16x32_f16 v[14:17], v[204:207], v[188:191], v[14:17]
	v_mfma_f32_16x16x32_f16 v[10:13], v[212:215], v[188:191], v[10:13]
	v_mfma_f32_16x16x32_f16 v[6:9], v[204:207], v[196:199], v[6:9]
	v_mfma_f32_16x16x32_f16 v[2:5], v[212:215], v[196:199], v[2:5]
	v_mfma_f32_16x16x32_f16 v[34:37], v[208:211], v[172:175], v[34:37]
	v_mfma_f32_16x16x32_f16 v[26:29], v[216:219], v[172:175], v[26:29]
	v_mfma_f32_16x16x32_f16 v[22:25], v[208:211], v[184:187], v[22:25]
	v_mfma_f32_16x16x32_f16 v[18:21], v[216:219], v[184:187], v[18:21]
	v_mfma_f32_16x16x32_f16 v[14:17], v[208:211], v[192:195], v[14:17]
	v_mfma_f32_16x16x32_f16 v[10:13], v[216:219], v[192:195], v[10:13]
	v_mfma_f32_16x16x32_f16 v[6:9], v[208:211], v[200:203], v[6:9]
	v_mfma_f32_16x16x32_f16 v[2:5], v[216:219], v[200:203], v[2:5]
	s_cmp_lt_u32 s57, 12
	s_mov_b32 s57, vcc_lo
	s_cbranch_scc1 .Lg2_head
	s_barrier
	s_add_u32 s34, s88, 0x780
	s_addc_u32 s35, s89, 0
	ds_read_b128 v[140:143], v138
	ds_read_b128 v[154:157], v138 offset:1024
	ds_read_b128 v[158:161], v138 offset:2048
	ds_read_b128 v[164:167], v138 offset:3072
	ds_read_b128 v[168:171], v134
	ds_read_b128 v[172:175], v134 offset:1024
	ds_read_b128 v[176:179], v133
	ds_read_b128 v[184:187], v133 offset:1024
	ds_read_b128 v[188:191], v131
	ds_read_b128 v[192:195], v131 offset:1024
	ds_read_b128 v[196:199], v130
	ds_read_b128 v[200:203], v130 offset:1024
	v_lshl_add_u64 v[138:139], s[34:35], 0, v[162:163]
	s_add_u32 s34, s34, 0x20000
	s_mov_b32 m0, s59
	s_addc_u32 s35, s35, 0
	global_load_lds_dwordx4 v[138:139], off
	s_mov_b32 m0, s58
	v_lshl_add_u64 v[138:139], s[34:35], 0, v[162:163]
	global_load_lds_dwordx4 v[138:139], off
	s_barrier
	s_waitcnt lgkmcnt(0)
	v_mfma_f32_16x16x32_f16 v[102:105], v[140:143], v[168:171], v[102:105]
	v_mfma_f32_16x16x32_f16 v[98:101], v[158:161], v[168:171], v[98:101]
	v_mfma_f32_16x16x32_f16 v[126:129], v[140:143], v[176:179], v[126:129]
	v_mfma_f32_16x16x32_f16 v[122:125], v[158:161], v[176:179], v[122:125]
	v_mfma_f32_16x16x32_f16 v[118:121], v[140:143], v[188:191], v[118:121]
	v_mfma_f32_16x16x32_f16 v[114:117], v[158:161], v[188:191], v[114:117]
	v_mfma_f32_16x16x32_f16 v[110:113], v[140:143], v[196:199], v[110:113]
	v_mfma_f32_16x16x32_f16 v[106:109], v[158:161], v[196:199], v[106:109]
	v_mfma_f32_16x16x32_f16 v[102:105], v[154:157], v[172:175], v[102:105]
	v_mfma_f32_16x16x32_f16 v[98:101], v[164:167], v[172:175], v[98:101]
	v_mfma_f32_16x16x32_f16 v[126:129], v[154:157], v[184:187], v[126:129]
	v_mfma_f32_16x16x32_f16 v[122:125], v[164:167], v[184:187], v[122:125]
	v_mfma_f32_16x16x32_f16 v[118:121], v[154:157], v[192:195], v[118:121]
	v_mfma_f32_16x16x32_f16 v[114:117], v[164:167], v[192:195], v[114:117]
	v_mfma_f32_16x16x32_f16 v[110:113], v[154:157], v[200:203], v[110:113]
	v_mfma_f32_16x16x32_f16 v[106:109], v[164:167], v[200:203], v[106:109]
	s_barrier
	ds_read_b128 v[204:207], v137
	ds_read_b128 v[208:211], v137 offset:1024
	ds_read_b128 v[212:215], v137 offset:2048
	ds_read_b128 v[216:219], v137 offset:3072
	s_barrier
	s_waitcnt lgkmcnt(0)
	v_mfma_f32_16x16x32_f16 v[94:97], v[204:207], v[168:171], v[94:97]
	v_mfma_f32_16x16x32_f16 v[94:97], v[208:211], v[172:175], v[94:97]
	v_mfma_f32_16x16x32_f16 v[90:93], v[212:215], v[168:171], v[90:93]
	v_mfma_f32_16x16x32_f16 v[86:89], v[204:207], v[176:179], v[86:89]
	v_mfma_f32_16x16x32_f16 v[82:85], v[212:215], v[176:179], v[82:85]
	v_mfma_f32_16x16x32_f16 v[78:81], v[204:207], v[188:191], v[78:81]
	v_mfma_f32_16x16x32_f16 v[74:77], v[212:215], v[188:191], v[74:77]
	v_mfma_f32_16x16x32_f16 v[70:73], v[204:207], v[196:199], v[70:73]
	v_mfma_f32_16x16x32_f16 v[66:69], v[212:215], v[196:199], v[66:69]
	v_mfma_f32_16x16x32_f16 v[168:171], v[216:219], v[172:175], v[90:93]
	v_mfma_f32_16x16x32_f16 v[172:175], v[208:211], v[184:187], v[86:89]
	v_mfma_f32_16x16x32_f16 v[176:179], v[216:219], v[184:187], v[82:85]
	v_mfma_f32_16x16x32_f16 v[184:187], v[208:211], v[192:195], v[78:81]
	v_mfma_f32_16x16x32_f16 v[188:191], v[216:219], v[192:195], v[74:77]
	v_mfma_f32_16x16x32_f16 v[192:195], v[208:211], v[200:203], v[70:73]
	v_mfma_f32_16x16x32_f16 v[196:199], v[216:219], v[200:203], v[66:69]
	s_barrier
	s_nop 0
	ds_read_b128 v[66:69], v134 offset:16384
	ds_read_b128 v[70:73], v134 offset:17408
	ds_read_b128 v[74:77], v133 offset:16384
	ds_read_b128 v[78:81], v133 offset:17408
	ds_read_b128 v[82:85], v131 offset:16384
	ds_read_b128 v[86:89], v131 offset:17408
	ds_read_b128 v[90:93], v130 offset:16384
	ds_read_b128 v[200:203], v130 offset:17408
	s_waitcnt vmcnt(4)
	s_barrier
	s_waitcnt lgkmcnt(0)
	v_mfma_f32_16x16x32_f16 v[62:65], v[140:143], v[66:69], v[62:65]
	v_mfma_f32_16x16x32_f16 v[58:61], v[158:161], v[66:69], v[58:61]
	v_mfma_f32_16x16x32_f16 v[54:57], v[140:143], v[74:77], v[54:57]
	v_mfma_f32_16x16x32_f16 v[50:53], v[158:161], v[74:77], v[50:53]
	v_mfma_f32_16x16x32_f16 v[46:49], v[140:143], v[82:85], v[46:49]
	v_mfma_f32_16x16x32_f16 v[42:45], v[158:161], v[82:85], v[42:45]
	v_mfma_f32_16x16x32_f16 v[38:41], v[140:143], v[90:93], v[38:41]
	v_mfma_f32_16x16x32_f16 v[62:65], v[154:157], v[70:73], v[62:65]
	v_mfma_f32_16x16x32_f16 v[58:61], v[164:167], v[70:73], v[58:61]
	v_mfma_f32_16x16x32_f16 v[54:57], v[154:157], v[78:81], v[54:57]
	v_mfma_f32_16x16x32_f16 v[50:53], v[164:167], v[78:81], v[50:53]
	v_mfma_f32_16x16x32_f16 v[46:49], v[154:157], v[86:89], v[46:49]
	v_mfma_f32_16x16x32_f16 v[42:45], v[164:167], v[86:89], v[42:45]
	v_mfma_f32_16x16x32_f16 v[38:41], v[154:157], v[200:203], v[38:41]
	v_mfma_f32_16x16x32_f16 v[30:33], v[158:161], v[90:93], v[30:33]
	v_mfma_f32_16x16x32_f16 v[138:141], v[164:167], v[200:203], v[30:33]
	v_mfma_f32_16x16x32_f16 v[30:33], v[204:207], v[66:69], v[34:37]
	v_mfma_f32_16x16x32_f16 v[34:37], v[208:211], v[70:73], v[30:33]
	v_mfma_f32_16x16x32_f16 v[26:29], v[212:215], v[66:69], v[26:29]
	v_mfma_f32_16x16x32_f16 v[22:25], v[204:207], v[74:77], v[22:25]
	v_mfma_f32_16x16x32_f16 v[18:21], v[212:215], v[74:77], v[18:21]
	v_mfma_f32_16x16x32_f16 v[14:17], v[204:207], v[82:85], v[14:17]
	v_mfma_f32_16x16x32_f16 v[10:13], v[212:215], v[82:85], v[10:13]
	v_mfma_f32_16x16x32_f16 v[6:9], v[204:207], v[90:93], v[6:9]
	v_mfma_f32_16x16x32_f16 v[2:5], v[212:215], v[90:93], v[2:5]
	v_mfma_f32_16x16x32_f16 v[142:145], v[216:219], v[70:73], v[26:29]
	v_mfma_f32_16x16x32_f16 v[154:157], v[208:211], v[78:81], v[22:25]
	v_mfma_f32_16x16x32_f16 v[158:161], v[216:219], v[78:81], v[18:21]
	v_mfma_f32_16x16x32_f16 v[164:167], v[208:211], v[86:89], v[14:17]
	v_mfma_f32_16x16x32_f16 v[220:223], v[216:219], v[86:89], v[10:13]
	v_mfma_f32_16x16x32_f16 v[204:207], v[208:211], v[200:203], v[6:9]
	v_mfma_f32_16x16x32_f16 v[200:203], v[216:219], v[200:203], v[2:5]
	s_barrier
	s_nop 0
	ds_read_b128 v[2:5], v136
	ds_read_b128 v[6:9], v136 offset:1024
	ds_read_b128 v[208:211], v136 offset:2048
	ds_read_b128 v[212:215], v136 offset:3072
	ds_read_b128 v[10:13], v134 offset:32768
	ds_read_b128 v[14:17], v134 offset:33792
	ds_read_b128 v[18:21], v133 offset:32768
	ds_read_b128 v[22:25], v133 offset:33792
	ds_read_b128 v[26:29], v131 offset:32768
	ds_read_b128 v[30:33], v131 offset:33792
	ds_read_b128 v[216:219], v130 offset:32768
	ds_read_b128 v[224:227], v130 offset:33792
	s_waitcnt vmcnt(2)
	s_barrier
	s_waitcnt lgkmcnt(0)
	v_mfma_f32_16x16x32_f16 v[66:69], v[2:5], v[10:13], v[102:105]
	v_mfma_f32_16x16x32_f16 v[90:93], v[6:9], v[14:17], v[66:69]
	v_mfma_f32_16x16x32_f16 v[66:69], v[208:211], v[10:13], v[98:101]
	v_mfma_f32_16x16x32_f16 v[98:101], v[212:215], v[14:17], v[66:69]
	v_mfma_f32_16x16x32_f16 v[66:69], v[2:5], v[18:21], v[126:129]
	v_mfma_f32_16x16x32_f16 v[82:85], v[6:9], v[22:25], v[66:69]
	v_mfma_f32_16x16x32_f16 v[66:69], v[208:211], v[18:21], v[122:125]
	v_mfma_f32_16x16x32_f16 v[86:89], v[212:215], v[22:25], v[66:69]
	v_mfma_f32_16x16x32_f16 v[66:69], v[2:5], v[26:29], v[118:121]
	v_mfma_f32_16x16x32_f16 v[74:77], v[6:9], v[30:33], v[66:69]
	v_mfma_f32_16x16x32_f16 v[66:69], v[208:211], v[26:29], v[114:117]
	v_mfma_f32_16x16x32_f16 v[78:81], v[212:215], v[30:33], v[66:69]
	v_mfma_f32_16x16x32_f16 v[66:69], v[2:5], v[216:219], v[110:113]
	v_mfma_f32_16x16x32_f16 v[70:73], v[208:211], v[216:219], v[106:109]
	v_mfma_f32_16x16x32_f16 v[66:69], v[6:9], v[224:227], v[66:69]
	v_mfma_f32_16x16x32_f16 v[70:73], v[212:215], v[224:227], v[70:73]
	s_barrier
	ds_read_b128 v[228:231], v135
	ds_read_b128 v[232:235], v135 offset:1024
	ds_read_b128 v[236:239], v135 offset:2048
	ds_read_b128 v[240:243], v135 offset:3072
	s_waitcnt vmcnt(0)
	s_barrier
	s_waitcnt lgkmcnt(0)
	v_mfma_f32_16x16x32_f16 v[94:97], v[228:231], v[10:13], v[94:97]
	v_mfma_f32_16x16x32_f16 v[10:13], v[236:239], v[10:13], v[168:171]
	v_mfma_f32_16x16x32_f16 v[126:129], v[240:243], v[14:17], v[10:13]
	v_mfma_f32_16x16x32_f16 v[10:13], v[228:231], v[18:21], v[172:175]
	v_mfma_f32_16x16x32_f16 v[114:117], v[232:235], v[22:25], v[10:13]
	v_mfma_f32_16x16x32_f16 v[10:13], v[236:239], v[18:21], v[176:179]
	v_mfma_f32_16x16x32_f16 v[118:121], v[240:243], v[22:25], v[10:13]
	v_mfma_f32_16x16x32_f16 v[10:13], v[228:231], v[26:29], v[184:187]
	v_mfma_f32_16x16x32_f16 v[106:109], v[232:235], v[30:33], v[10:13]
	v_mfma_f32_16x16x32_f16 v[10:13], v[236:239], v[26:29], v[188:191]
	v_mfma_f32_16x16x32_f16 v[110:113], v[240:243], v[30:33], v[10:13]
	v_mfma_f32_16x16x32_f16 v[10:13], v[228:231], v[216:219], v[192:195]
	v_mfma_f32_16x16x32_f16 v[122:125], v[232:235], v[14:17], v[94:97]
	v_mfma_f32_16x16x32_f16 v[94:97], v[232:235], v[224:227], v[10:13]
	v_mfma_f32_16x16x32_f16 v[10:13], v[236:239], v[216:219], v[196:199]
	v_mfma_f32_16x16x32_f16 v[102:105], v[240:243], v[224:227], v[10:13]
	s_barrier
	ds_read_b128 v[168:171], v134 offset:49152
	ds_read_b128 v[134:137], v134 offset:50176
	ds_read_b128 v[172:175], v133 offset:49152
	ds_read_b128 v[176:179], v133 offset:50176
	ds_read_b128 v[184:187], v131 offset:49152
	ds_read_b128 v[188:191], v131 offset:50176
	ds_read_b128 v[192:195], v130 offset:49152
	ds_read_b128 v[196:199], v130 offset:50176
	s_barrier
	s_waitcnt lgkmcnt(0)
	v_mfma_f32_16x16x32_f16 v[10:13], v[2:5], v[168:171], v[62:65]
	v_mfma_f32_16x16x32_f16 v[26:29], v[6:9], v[134:137], v[10:13]
	v_mfma_f32_16x16x32_f16 v[10:13], v[208:211], v[168:171], v[58:61]
	v_mfma_f32_16x16x32_f16 v[30:33], v[212:215], v[134:137], v[10:13]
	v_mfma_f32_16x16x32_f16 v[10:13], v[2:5], v[172:175], v[54:57]
	v_mfma_f32_16x16x32_f16 v[18:21], v[6:9], v[176:179], v[10:13]
	v_mfma_f32_16x16x32_f16 v[10:13], v[208:211], v[172:175], v[50:53]
	v_mfma_f32_16x16x32_f16 v[22:25], v[212:215], v[176:179], v[10:13]
	v_mfma_f32_16x16x32_f16 v[10:13], v[2:5], v[184:187], v[46:49]
	v_mfma_f32_16x16x32_f16 v[2:5], v[2:5], v[192:195], v[38:41]
	v_mfma_f32_16x16x32_f16 v[10:13], v[6:9], v[188:191], v[10:13]
	v_mfma_f32_16x16x32_f16 v[14:17], v[208:211], v[184:187], v[42:45]
	v_mfma_f32_16x16x32_f16 v[2:5], v[6:9], v[196:199], v[2:5]
	v_mfma_f32_16x16x32_f16 v[6:9], v[208:211], v[192:195], v[138:141]
	v_mfma_f32_16x16x32_f16 v[14:17], v[212:215], v[188:191], v[14:17]
	v_mfma_f32_16x16x32_f16 v[6:9], v[212:215], v[196:199], v[6:9]
	v_mfma_f32_16x16x32_f16 v[34:37], v[228:231], v[168:171], v[34:37]
	v_mfma_f32_16x16x32_f16 v[58:61], v[232:235], v[134:137], v[34:37]
	v_mfma_f32_16x16x32_f16 v[34:37], v[236:239], v[168:171], v[142:145]
	v_mfma_f32_16x16x32_f16 v[62:65], v[240:243], v[134:137], v[34:37]
	v_mfma_f32_16x16x32_f16 v[34:37], v[228:231], v[172:175], v[154:157]
	v_mfma_f32_16x16x32_f16 v[50:53], v[232:235], v[176:179], v[34:37]
	v_mfma_f32_16x16x32_f16 v[34:37], v[236:239], v[172:175], v[158:161]
	v_mfma_f32_16x16x32_f16 v[54:57], v[240:243], v[176:179], v[34:37]
	v_mfma_f32_16x16x32_f16 v[34:37], v[228:231], v[184:187], v[164:167]
	v_mfma_f32_16x16x32_f16 v[42:45], v[232:235], v[188:191], v[34:37]
	v_mfma_f32_16x16x32_f16 v[34:37], v[236:239], v[184:187], v[220:223]
	v_mfma_f32_16x16x32_f16 v[46:49], v[240:243], v[188:191], v[34:37]
	v_mfma_f32_16x16x32_f16 v[34:37], v[228:231], v[192:195], v[204:207]
	v_mfma_f32_16x16x32_f16 v[38:41], v[236:239], v[192:195], v[200:203]
	v_mfma_f32_16x16x32_f16 v[34:37], v[232:235], v[196:199], v[34:37]
	v_mfma_f32_16x16x32_f16 v[38:41], v[240:243], v[196:199], v[38:41]

.LBB2_381:
	s_or_b64 exec, exec, s[34:35]
	s_add_u32 s34, s4, 0x80
	s_addc_u32 s35, s5, 0
	s_add_i32 s58, 0, 0x18000
	s_add_i32 s56, s58, s33
	v_lshl_add_u64 v[4:5], s[34:35], 0, v[162:163]
	s_add_u32 s34, s34, 0x40000
	s_mov_b32 m0, s56
	s_addc_u32 s35, s35, 0
	s_waitcnt vmcnt(4)
	s_barrier
	global_load_lds_dwordx4 v[4:5], off
	s_add_i32 m0, s56, 0x2000
	v_readlane_b32 s56, v244, 6
	v_mov_b32_e32 v135, v163
	v_lshl_add_u64 v[4:5], s[34:35], 0, v[162:163]
	v_readlane_b32 s57, v244, 7
	s_add_i32 s34, s52, 0x8000
	v_mov_b32_e32 v137, v163
	global_load_lds_dwordx4 v[4:5], off
	s_mov_b32 m0, s34
	v_lshl_add_u64 v[4:5], s[56:57], 0, v[134:135]
	s_add_i32 s35, s52, 0xa000
	global_load_lds_dwordx4 v[4:5], off
	v_lshl_add_u64 v[4:5], s[56:57], 0, v[136:137]
	s_add_u32 s56, s4, 0x80080
	s_addc_u32 s57, s5, 0
	s_add_i32 s59, 0, 0x1c000
	s_mov_b32 m0, s35
	s_add_i32 s33, s59, s33
	global_load_lds_dwordx4 v[4:5], off
	v_lshl_add_u64 v[4:5], s[56:57], 0, v[162:163]
	s_add_u32 s56, s56, 0x40000
	s_mov_b32 m0, s33
	s_addc_u32 s57, s57, 0
	global_load_lds_dwordx4 v[4:5], off
	s_add_i32 m0, s33, 0x2000
	v_lshl_add_u64 v[4:5], s[56:57], 0, v[162:163]
	global_load_lds_dwordx4 v[4:5], off
	v_and_b32_e32 v139, 15, v141
	v_bfe_u32 v140, v141, 4, 2
	v_lshlrev_b32_e32 v6, 2, v141
	v_lshlrev_b32_e32 v4, 4, v140
	v_lshlrev_b32_e32 v5, 6, v139
	v_and_b32_e32 v6, 32, v6
	v_bitop3_b32 v5, v4, v6, v5 bitop3:0x36
	s_add_i32 s33, 0, 0x10000
	v_add_u32_e32 v7, s33, v5
	s_add_i32 s33, 0, 0x14000
	v_lshlrev_b32_e32 v143, 6, v2
	v_add_u32_e32 v8, s33, v5
	v_lshlrev_b32_e32 v11, 13, v2
	v_lshlrev_b32_e32 v2, 6, v141
	s_movk_i32 s33, 0x3c0
	v_and_b32_e32 v142, 3, v138
	s_waitcnt vmcnt(6)
	v_and_or_b32 v2, v2, s33, v4
	v_lshlrev_b32_e32 v3, 12, v142
	v_add_u32_e32 v9, s58, v5
	v_add_u32_e32 v10, s59, v5
	v_add_u32_e32 v5, 0, v5
	v_xad_u32 v4, v2, v6, 0
	v_or_b32_e32 v6, 0x800, v11
	v_or_b32_e32 v12, 0x1000, v11
	v_or_b32_e32 v13, 0x1800, v11
	v_mov_b32_e32 v2, 0
	s_mov_b32 s84, 0
	v_add_u32_e32 v151, v7, v3
	v_add_u32_e32 v147, v5, v11
	v_add_u32_e32 v146, v4, v6
	v_add_u32_e32 v145, v4, v12
	v_add_u32_e32 v144, v4, v13
	v_add_u32_e32 v150, v8, v3
	v_add_u32_e32 v149, v9, v3
	v_add_u32_e32 v148, v10, v3
	v_mov_b32_e32 v3, v2
	v_mov_b32_e32 v4, v2
	v_mov_b32_e32 v5, v2
	v_mov_b32_e32 v6, v2
	v_mov_b32_e32 v7, v2
	v_mov_b32_e32 v8, v2
	v_mov_b32_e32 v9, v2
	v_mov_b32_e32 v10, v2
	v_mov_b32_e32 v11, v2
	v_mov_b32_e32 v12, v2
	v_mov_b32_e32 v13, v2
	v_mov_b32_e32 v14, v2
	v_mov_b32_e32 v15, v2
	v_mov_b32_e32 v16, v2
	v_mov_b32_e32 v17, v2
	v_mov_b32_e32 v18, v2
	v_mov_b32_e32 v19, v2
	v_mov_b32_e32 v20, v2
	v_mov_b32_e32 v21, v2
	v_mov_b32_e32 v22, v2
	v_mov_b32_e32 v23, v2
	v_mov_b32_e32 v24, v2
	v_mov_b32_e32 v25, v2
	v_mov_b32_e32 v26, v2
	v_mov_b32_e32 v27, v2
	v_mov_b32_e32 v28, v2
	v_mov_b32_e32 v29, v2
	v_mov_b32_e32 v30, v2
	v_mov_b32_e32 v31, v2
	v_mov_b32_e32 v32, v2
	v_mov_b32_e32 v33, v2
	v_mov_b32_e32 v34, v2
	v_mov_b32_e32 v35, v2
	v_mov_b32_e32 v36, v2
	v_mov_b32_e32 v37, v2
	v_mov_b32_e32 v38, v2
	v_mov_b32_e32 v39, v2
	v_mov_b32_e32 v40, v2
	v_mov_b32_e32 v41, v2
	v_mov_b32_e32 v42, v2
	v_mov_b32_e32 v43, v2
	v_mov_b32_e32 v44, v2
	v_mov_b32_e32 v45, v2
	v_mov_b32_e32 v46, v2
	v_mov_b32_e32 v47, v2
	v_mov_b32_e32 v48, v2
	v_mov_b32_e32 v49, v2
	v_mov_b32_e32 v50, v2
	v_mov_b32_e32 v51, v2
	v_mov_b32_e32 v52, v2
	v_mov_b32_e32 v53, v2
	v_mov_b32_e32 v54, v2
	v_mov_b32_e32 v55, v2
	v_mov_b32_e32 v56, v2
	v_mov_b32_e32 v57, v2
	v_mov_b32_e32 v58, v2
	v_mov_b32_e32 v59, v2
	v_mov_b32_e32 v60, v2
	v_mov_b32_e32 v61, v2
	v_mov_b32_e32 v62, v2
	v_mov_b32_e32 v63, v2
	v_mov_b32_e32 v64, v2
	v_mov_b32_e32 v65, v2
	v_mov_b32_e32 v66, v2
	v_mov_b32_e32 v67, v2
	v_mov_b32_e32 v68, v2
	v_mov_b32_e32 v69, v2
	v_mov_b32_e32 v70, v2
	v_mov_b32_e32 v71, v2
	v_mov_b32_e32 v72, v2
	v_mov_b32_e32 v73, v2
	v_mov_b32_e32 v74, v2
	v_mov_b32_e32 v75, v2
	v_mov_b32_e32 v76, v2
	v_mov_b32_e32 v77, v2
	v_mov_b32_e32 v78, v2
	v_mov_b32_e32 v79, v2
	v_mov_b32_e32 v80, v2
	v_mov_b32_e32 v81, v2
	v_mov_b32_e32 v82, v2
	v_mov_b32_e32 v83, v2
	v_mov_b32_e32 v84, v2
	v_mov_b32_e32 v85, v2
	v_mov_b32_e32 v86, v2
	v_mov_b32_e32 v87, v2
	v_mov_b32_e32 v88, v2
	v_mov_b32_e32 v89, v2
	v_mov_b32_e32 v90, v2
	v_mov_b32_e32 v91, v2
	v_mov_b32_e32 v92, v2
	v_mov_b32_e32 v93, v2
	v_mov_b32_e32 v94, v2
	v_mov_b32_e32 v95, v2
	v_mov_b32_e32 v96, v2
	v_mov_b32_e32 v97, v2
	v_mov_b32_e32 v98, v2
	v_mov_b32_e32 v99, v2
	v_mov_b32_e32 v100, v2
	v_mov_b32_e32 v101, v2
	v_mov_b32_e32 v102, v2
	v_mov_b32_e32 v103, v2
	v_mov_b32_e32 v104, v2
	v_mov_b32_e32 v105, v2
	v_mov_b32_e32 v106, v2
	v_mov_b32_e32 v107, v2
	v_mov_b32_e32 v108, v2
	v_mov_b32_e32 v109, v2
	v_mov_b32_e32 v110, v2
	v_mov_b32_e32 v111, v2
	v_mov_b32_e32 v112, v2
	v_mov_b32_e32 v113, v2
	v_mov_b32_e32 v114, v2
	v_mov_b32_e32 v115, v2
	v_mov_b32_e32 v116, v2
	v_mov_b32_e32 v117, v2
	v_mov_b32_e32 v118, v2
	v_mov_b32_e32 v119, v2
	v_mov_b32_e32 v120, v2
	v_mov_b32_e32 v121, v2
	v_mov_b32_e32 v122, v2
	v_mov_b32_e32 v123, v2
	v_mov_b32_e32 v124, v2
	v_mov_b32_e32 v125, v2
	v_mov_b32_e32 v126, v2
	v_mov_b32_e32 v127, v2
	v_mov_b32_e32 v128, v2
	v_mov_b32_e32 v129, v2
	v_mov_b32_e32 v133, v163
	v_mov_b32_e32 v131, v163
	s_barrier
	s_cmp_lg_u32 s100, 0
	s_cbranch_scc1 .Lg1p_loop
	s_branch .LBB2_382

.LBB2_382:
	ds_read_b128 v[152:155], v151
	ds_read_b128 v[156:159], v151 offset:1024
	ds_read_b128 v[164:167], v151 offset:2048
	ds_read_b128 v[168:171], v151 offset:3072
	s_lshl_b32 s58, s84, 7
	s_add_u32 s59, s24, s58
	s_addc_u32 s91, s25, 0
	s_add_u32 s92, s59, 0x80
	s_addc_u32 s93, s91, 0
	s_add_i32 s56, s52, 0xc000
	s_mov_b32 m0, s56
	s_add_i32 s33, s52, 0xe000
	ds_read_b128 v[172:175], v147
	ds_read_b128 v[176:179], v147 offset:1024
	ds_read_b128 v[184:187], v146
	ds_read_b128 v[188:191], v146 offset:1024
	ds_read_b128 v[192:195], v145
	ds_read_b128 v[196:199], v145 offset:1024
	ds_read_b128 v[200:203], v144
	ds_read_b128 v[204:207], v144 offset:1024
	global_load_lds_dwordx4 v132, s[92:93]
	s_mov_b32 m0, s33
	s_nop 0
	global_load_lds_dwordx4 v130, s[92:93]
	s_waitcnt lgkmcnt(8)
	s_barrier
	s_waitcnt lgkmcnt(0)
	v_mfma_f32_16x16x32_f16 v[126:129], v[152:155], v[172:175], v[126:129]
	v_mfma_f32_16x16x32_f16 v[122:125], v[164:167], v[172:175], v[122:125]
	v_mfma_f32_16x16x32_f16 v[118:121], v[152:155], v[184:187], v[118:121]
	v_mfma_f32_16x16x32_f16 v[114:117], v[164:167], v[184:187], v[114:117]
	v_mfma_f32_16x16x32_f16 v[110:113], v[152:155], v[192:195], v[110:113]
	v_mfma_f32_16x16x32_f16 v[106:109], v[164:167], v[192:195], v[106:109]
	v_mfma_f32_16x16x32_f16 v[102:105], v[152:155], v[200:203], v[102:105]
	v_mfma_f32_16x16x32_f16 v[98:101], v[164:167], v[200:203], v[98:101]
	v_mfma_f32_16x16x32_f16 v[126:129], v[156:159], v[176:179], v[126:129]
	v_mfma_f32_16x16x32_f16 v[122:125], v[168:171], v[176:179], v[122:125]
	v_mfma_f32_16x16x32_f16 v[118:121], v[156:159], v[188:191], v[118:121]
	v_mfma_f32_16x16x32_f16 v[114:117], v[168:171], v[188:191], v[114:117]
	v_mfma_f32_16x16x32_f16 v[110:113], v[156:159], v[196:199], v[110:113]
	v_mfma_f32_16x16x32_f16 v[106:109], v[168:171], v[196:199], v[106:109]
	v_mfma_f32_16x16x32_f16 v[102:105], v[156:159], v[204:207], v[102:105]
	v_mfma_f32_16x16x32_f16 v[98:101], v[168:171], v[204:207], v[98:101]
	s_barrier
	s_add_i32 s57, s84, 2
	s_lshl_b32 s82, s57, 7
	s_add_u32 s92, s4, s82
	s_addc_u32 s93, s5, 0
	s_mov_b32 m0, s53
	ds_read_b128 v[208:211], v150
	ds_read_b128 v[212:215], v150 offset:1024
	ds_read_b128 v[216:219], v150 offset:2048
	ds_read_b128 v[220:223], v150 offset:3072
	global_load_lds_dwordx4 v162, s[92:93]
	s_mov_b32 m0, s55
	s_add_u32 s92, s92, 0x40000
	s_addc_u32 s93, s93, 0
	global_load_lds_dwordx4 v162, s[92:93]
	s_barrier
	s_waitcnt lgkmcnt(0)
	v_mfma_f32_16x16x32_f16 v[94:97], v[208:211], v[172:175], v[94:97]
	v_mfma_f32_16x16x32_f16 v[90:93], v[216:219], v[172:175], v[90:93]
	v_mfma_f32_16x16x32_f16 v[86:89], v[208:211], v[184:187], v[86:89]
	v_mfma_f32_16x16x32_f16 v[82:85], v[216:219], v[184:187], v[82:85]
	v_mfma_f32_16x16x32_f16 v[78:81], v[208:211], v[192:195], v[78:81]
	v_mfma_f32_16x16x32_f16 v[74:77], v[216:219], v[192:195], v[74:77]
	v_mfma_f32_16x16x32_f16 v[70:73], v[208:211], v[200:203], v[70:73]
	v_mfma_f32_16x16x32_f16 v[66:69], v[216:219], v[200:203], v[66:69]
	v_mfma_f32_16x16x32_f16 v[94:97], v[212:215], v[176:179], v[94:97]
	v_mfma_f32_16x16x32_f16 v[90:93], v[220:223], v[176:179], v[90:93]
	v_mfma_f32_16x16x32_f16 v[86:89], v[212:215], v[188:191], v[86:89]
	v_mfma_f32_16x16x32_f16 v[82:85], v[220:223], v[188:191], v[82:85]
	v_mfma_f32_16x16x32_f16 v[78:81], v[212:215], v[196:199], v[78:81]
	v_mfma_f32_16x16x32_f16 v[74:77], v[220:223], v[196:199], v[74:77]
	v_mfma_f32_16x16x32_f16 v[70:73], v[212:215], v[204:207], v[70:73]
	v_mfma_f32_16x16x32_f16 v[66:69], v[220:223], v[204:207], v[66:69]
	s_add_u32 s92, s24, s82
	s_addc_u32 s93, s25, 0
	s_mov_b32 m0, s52
	s_barrier
	ds_read_b128 v[172:175], v147 offset:16384
	ds_read_b128 v[176:179], v147 offset:17408
	ds_read_b128 v[184:187], v146 offset:16384
	ds_read_b128 v[188:191], v146 offset:17408
	ds_read_b128 v[192:195], v145 offset:16384
	ds_read_b128 v[196:199], v145 offset:17408
	ds_read_b128 v[200:203], v144 offset:16384
	ds_read_b128 v[204:207], v144 offset:17408
	global_load_lds_dwordx4 v134, s[92:93]
	s_mov_b32 m0, s86
	s_nop 0
	global_load_lds_dwordx4 v136, s[92:93]
	s_barrier
	s_waitcnt lgkmcnt(0)
	v_mfma_f32_16x16x32_f16 v[62:65], v[152:155], v[172:175], v[62:65]
	v_mfma_f32_16x16x32_f16 v[58:61], v[164:167], v[172:175], v[58:61]
	v_mfma_f32_16x16x32_f16 v[54:57], v[152:155], v[184:187], v[54:57]
	v_mfma_f32_16x16x32_f16 v[50:53], v[164:167], v[184:187], v[50:53]
	v_mfma_f32_16x16x32_f16 v[46:49], v[152:155], v[192:195], v[46:49]
	v_mfma_f32_16x16x32_f16 v[42:45], v[164:167], v[192:195], v[42:45]
	v_mfma_f32_16x16x32_f16 v[38:41], v[152:155], v[200:203], v[38:41]
	v_mfma_f32_16x16x32_f16 v[34:37], v[164:167], v[200:203], v[34:37]
	v_mfma_f32_16x16x32_f16 v[62:65], v[156:159], v[176:179], v[62:65]
	v_mfma_f32_16x16x32_f16 v[58:61], v[168:171], v[176:179], v[58:61]
	v_mfma_f32_16x16x32_f16 v[54:57], v[156:159], v[188:191], v[54:57]
	v_mfma_f32_16x16x32_f16 v[50:53], v[168:171], v[188:191], v[50:53]
	v_mfma_f32_16x16x32_f16 v[46:49], v[156:159], v[196:199], v[46:49]
	v_mfma_f32_16x16x32_f16 v[42:45], v[168:171], v[196:199], v[42:45]
	v_mfma_f32_16x16x32_f16 v[38:41], v[156:159], v[204:207], v[38:41]
	v_mfma_f32_16x16x32_f16 v[34:37], v[168:171], v[204:207], v[34:37]
	s_barrier
	s_add_u32 s94, s10, s82
	s_addc_u32 s95, s11, 0
	s_mov_b32 m0, s87
	s_nop 0
	global_load_lds_dwordx4 v162, s[94:95]
	s_mov_b32 m0, s88
	s_add_u32 s94, s94, 0x40000
	s_addc_u32 s95, s95, 0
	global_load_lds_dwordx4 v162, s[94:95]
	s_waitcnt vmcnt(6)
	s_barrier
	v_mfma_f32_16x16x32_f16 v[30:33], v[208:211], v[172:175], v[30:33]
	v_mfma_f32_16x16x32_f16 v[26:29], v[216:219], v[172:175], v[26:29]
	v_mfma_f32_16x16x32_f16 v[22:25], v[208:211], v[184:187], v[22:25]
	v_mfma_f32_16x16x32_f16 v[18:21], v[216:219], v[184:187], v[18:21]
	v_mfma_f32_16x16x32_f16 v[14:17], v[208:211], v[192:195], v[14:17]
	v_mfma_f32_16x16x32_f16 v[10:13], v[216:219], v[192:195], v[10:13]
	v_mfma_f32_16x16x32_f16 v[6:9], v[208:211], v[200:203], v[6:9]
	v_mfma_f32_16x16x32_f16 v[2:5], v[216:219], v[200:203], v[2:5]
	v_mfma_f32_16x16x32_f16 v[30:33], v[212:215], v[176:179], v[30:33]
	v_mfma_f32_16x16x32_f16 v[26:29], v[220:223], v[176:179], v[26:29]
	v_mfma_f32_16x16x32_f16 v[22:25], v[212:215], v[188:191], v[22:25]
	v_mfma_f32_16x16x32_f16 v[18:21], v[220:223], v[188:191], v[18:21]
	v_mfma_f32_16x16x32_f16 v[14:17], v[212:215], v[196:199], v[14:17]
	v_mfma_f32_16x16x32_f16 v[10:13], v[220:223], v[196:199], v[10:13]
	v_mfma_f32_16x16x32_f16 v[6:9], v[212:215], v[204:207], v[6:9]
	v_mfma_f32_16x16x32_f16 v[2:5], v[220:223], v[204:207], v[2:5]
	s_barrier
	ds_read_b128 v[152:155], v149
	ds_read_b128 v[156:159], v149 offset:1024
	ds_read_b128 v[164:167], v149 offset:2048
	ds_read_b128 v[168:171], v149 offset:3072
	s_mov_b32 m0, s89
	ds_read_b128 v[172:175], v147 offset:32768
	ds_read_b128 v[176:179], v147 offset:33792
	ds_read_b128 v[184:187], v146 offset:32768
	ds_read_b128 v[188:191], v146 offset:33792
	ds_read_b128 v[192:195], v145 offset:32768
	ds_read_b128 v[196:199], v145 offset:33792
	ds_read_b128 v[200:203], v144 offset:32768
	ds_read_b128 v[204:207], v144 offset:33792
	global_load_lds_dwordx4 v132, s[92:93]
	s_mov_b32 m0, s90
	s_nop 0
	global_load_lds_dwordx4 v130, s[92:93]
	s_waitcnt lgkmcnt(8)
	s_barrier
	s_waitcnt lgkmcnt(0)
	v_mfma_f32_16x16x32_f16 v[126:129], v[152:155], v[172:175], v[126:129]
	v_mfma_f32_16x16x32_f16 v[122:125], v[164:167], v[172:175], v[122:125]
	v_mfma_f32_16x16x32_f16 v[118:121], v[152:155], v[184:187], v[118:121]
	v_mfma_f32_16x16x32_f16 v[114:117], v[164:167], v[184:187], v[114:117]
	v_mfma_f32_16x16x32_f16 v[110:113], v[152:155], v[192:195], v[110:113]
	v_mfma_f32_16x16x32_f16 v[106:109], v[164:167], v[192:195], v[106:109]
	v_mfma_f32_16x16x32_f16 v[102:105], v[152:155], v[200:203], v[102:105]
	v_mfma_f32_16x16x32_f16 v[98:101], v[164:167], v[200:203], v[98:101]
	v_mfma_f32_16x16x32_f16 v[126:129], v[156:159], v[176:179], v[126:129]
	v_mfma_f32_16x16x32_f16 v[122:125], v[168:171], v[176:179], v[122:125]
	v_mfma_f32_16x16x32_f16 v[118:121], v[156:159], v[188:191], v[118:121]
	v_mfma_f32_16x16x32_f16 v[114:117], v[168:171], v[188:191], v[114:117]
	v_mfma_f32_16x16x32_f16 v[110:113], v[156:159], v[196:199], v[110:113]
	v_mfma_f32_16x16x32_f16 v[106:109], v[168:171], v[196:199], v[106:109]
	v_mfma_f32_16x16x32_f16 v[102:105], v[156:159], v[204:207], v[102:105]
	v_mfma_f32_16x16x32_f16 v[98:101], v[168:171], v[204:207], v[98:101]
	s_barrier
	s_add_u32 s82, s4, s58
	s_addc_u32 s83, s5, 0
	s_add_u32 s92, s82, 0x180
	s_addc_u32 s93, s83, 0
	s_add_i32 m0, s52, 0x18000
	ds_read_b128 v[208:211], v148
	ds_read_b128 v[212:215], v148 offset:1024
	ds_read_b128 v[216:219], v148 offset:2048
	ds_read_b128 v[220:223], v148 offset:3072
	global_load_lds_dwordx4 v162, s[92:93]
	s_add_i32 m0, s52, 0x1a000
	s_add_u32 s92, s92, 0x40000
	s_addc_u32 s93, s93, 0
	global_load_lds_dwordx4 v162, s[92:93]
	s_barrier
	s_waitcnt lgkmcnt(0)
	v_mfma_f32_16x16x32_f16 v[94:97], v[208:211], v[172:175], v[94:97]
	v_mfma_f32_16x16x32_f16 v[90:93], v[216:219], v[172:175], v[90:93]
	v_mfma_f32_16x16x32_f16 v[86:89], v[208:211], v[184:187], v[86:89]
	v_mfma_f32_16x16x32_f16 v[82:85], v[216:219], v[184:187], v[82:85]
	v_mfma_f32_16x16x32_f16 v[78:81], v[208:211], v[192:195], v[78:81]
	v_mfma_f32_16x16x32_f16 v[74:77], v[216:219], v[192:195], v[74:77]
	v_mfma_f32_16x16x32_f16 v[70:73], v[208:211], v[200:203], v[70:73]
	v_mfma_f32_16x16x32_f16 v[66:69], v[216:219], v[200:203], v[66:69]
	v_mfma_f32_16x16x32_f16 v[94:97], v[212:215], v[176:179], v[94:97]
	v_mfma_f32_16x16x32_f16 v[90:93], v[220:223], v[176:179], v[90:93]
	v_mfma_f32_16x16x32_f16 v[86:89], v[212:215], v[188:191], v[86:89]
	v_mfma_f32_16x16x32_f16 v[82:85], v[220:223], v[188:191], v[82:85]
	v_mfma_f32_16x16x32_f16 v[78:81], v[212:215], v[196:199], v[78:81]
	v_mfma_f32_16x16x32_f16 v[74:77], v[220:223], v[196:199], v[74:77]
	v_mfma_f32_16x16x32_f16 v[70:73], v[212:215], v[204:207], v[70:73]
	v_mfma_f32_16x16x32_f16 v[66:69], v[220:223], v[204:207], v[66:69]
	s_add_u32 s92, s59, 0x180
	s_addc_u32 s93, s91, 0
	s_mov_b32 m0, s34
	s_barrier
	ds_read_b128 v[172:175], v147 offset:49152
	ds_read_b128 v[176:179], v147 offset:50176
	ds_read_b128 v[184:187], v146 offset:49152
	ds_read_b128 v[188:191], v146 offset:50176
	ds_read_b128 v[192:195], v145 offset:49152
	ds_read_b128 v[196:199], v145 offset:50176
	ds_read_b128 v[200:203], v144 offset:49152
	ds_read_b128 v[204:207], v144 offset:50176
	global_load_lds_dwordx4 v134, s[92:93]
	s_mov_b32 m0, s35
	s_nop 0
	global_load_lds_dwordx4 v136, s[92:93]
	s_barrier
	s_waitcnt lgkmcnt(0)
	v_mfma_f32_16x16x32_f16 v[62:65], v[152:155], v[172:175], v[62:65]
	v_mfma_f32_16x16x32_f16 v[58:61], v[164:167], v[172:175], v[58:61]
	v_mfma_f32_16x16x32_f16 v[54:57], v[152:155], v[184:187], v[54:57]
	v_mfma_f32_16x16x32_f16 v[50:53], v[164:167], v[184:187], v[50:53]
	v_mfma_f32_16x16x32_f16 v[46:49], v[152:155], v[192:195], v[46:49]
	v_mfma_f32_16x16x32_f16 v[42:45], v[164:167], v[192:195], v[42:45]
	v_mfma_f32_16x16x32_f16 v[38:41], v[152:155], v[200:203], v[38:41]
	v_mfma_f32_16x16x32_f16 v[34:37], v[164:167], v[200:203], v[34:37]
	v_mfma_f32_16x16x32_f16 v[62:65], v[156:159], v[176:179], v[62:65]
	v_mfma_f32_16x16x32_f16 v[58:61], v[168:171], v[176:179], v[58:61]
	v_mfma_f32_16x16x32_f16 v[54:57], v[156:159], v[188:191], v[54:57]
	v_mfma_f32_16x16x32_f16 v[50:53], v[168:171], v[188:191], v[50:53]
	v_mfma_f32_16x16x32_f16 v[46:49], v[156:159], v[196:199], v[46:49]
	v_mfma_f32_16x16x32_f16 v[42:45], v[168:171], v[196:199], v[42:45]
	v_mfma_f32_16x16x32_f16 v[38:41], v[156:159], v[204:207], v[38:41]
	v_mfma_f32_16x16x32_f16 v[34:37], v[168:171], v[204:207], v[34:37]
	s_barrier
	s_add_u32 s58, s10, s58
	s_addc_u32 s59, s11, 0
	s_add_u32 s58, s58, 0x180
	s_addc_u32 s59, s59, 0
	s_add_i32 m0, s52, 0x1c000
	s_nop 0
	global_load_lds_dwordx4 v162, s[58:59]
	s_add_i32 m0, s52, 0x1e000
	s_add_u32 s58, s58, 0x40000
	s_addc_u32 s59, s59, 0
	global_load_lds_dwordx4 v162, s[58:59]
	s_waitcnt vmcnt(6)
	s_barrier
	v_mfma_f32_16x16x32_f16 v[30:33], v[208:211], v[172:175], v[30:33]
	v_mfma_f32_16x16x32_f16 v[26:29], v[216:219], v[172:175], v[26:29]
	v_mfma_f32_16x16x32_f16 v[22:25], v[208:211], v[184:187], v[22:25]
	v_mfma_f32_16x16x32_f16 v[18:21], v[216:219], v[184:187], v[18:21]
	v_mfma_f32_16x16x32_f16 v[14:17], v[208:211], v[192:195], v[14:17]
	v_mfma_f32_16x16x32_f16 v[10:13], v[216:219], v[192:195], v[10:13]
	v_mfma_f32_16x16x32_f16 v[6:9], v[208:211], v[200:203], v[6:9]
	v_mfma_f32_16x16x32_f16 v[2:5], v[216:219], v[200:203], v[2:5]
	v_mfma_f32_16x16x32_f16 v[30:33], v[212:215], v[176:179], v[30:33]
	v_mfma_f32_16x16x32_f16 v[26:29], v[220:223], v[176:179], v[26:29]
	v_mfma_f32_16x16x32_f16 v[22:25], v[212:215], v[188:191], v[22:25]
	v_mfma_f32_16x16x32_f16 v[18:21], v[220:223], v[188:191], v[18:21]
	v_mfma_f32_16x16x32_f16 v[14:17], v[212:215], v[196:199], v[14:17]
	v_mfma_f32_16x16x32_f16 v[10:13], v[220:223], v[196:199], v[10:13]
	v_mfma_f32_16x16x32_f16 v[6:9], v[212:215], v[204:207], v[6:9]
	v_mfma_f32_16x16x32_f16 v[2:5], v[220:223], v[204:207], v[2:5]
	s_cmp_lt_u32 s84, 28
	s_mov_b32 s84, s57
	s_cbranch_scc1 .Lg1_head
	s_barrier
	v_readlane_b32 s4, v244, 8
	v_readlane_b32 s5, v244, 9
	s_mov_b32 m0, s56
	ds_read_b128 v[134:137], v151
	ds_read_b128 v[152:155], v151 offset:1024
	ds_read_b128 v[156:159], v151 offset:2048
	ds_read_b128 v[164:167], v151 offset:3072
	ds_read_b128 v[168:171], v147
	ds_read_b128 v[172:175], v147 offset:1024
	ds_read_b128 v[176:179], v146
	ds_read_b128 v[184:187], v146 offset:1024
	ds_read_b128 v[188:191], v145
	ds_read_b128 v[192:195], v145 offset:1024
	ds_read_b128 v[196:199], v144
	ds_read_b128 v[200:203], v144 offset:1024
	v_lshl_add_u64 v[132:133], s[4:5], 0, v[132:133]
	global_load_lds_dwordx4 v[132:133], off
	v_lshl_add_u64 v[130:131], s[4:5], 0, v[130:131]
	s_mov_b32 m0, s33
	s_nop 0
	global_load_lds_dwordx4 v[130:131], off
	s_barrier
	s_waitcnt lgkmcnt(0)
	v_mfma_f32_16x16x32_f16 v[126:129], v[134:137], v[168:171], v[126:129]
	v_mfma_f32_16x16x32_f16 v[122:125], v[156:159], v[168:171], v[122:125]
	v_mfma_f32_16x16x32_f16 v[110:113], v[134:137], v[188:191], v[110:113]
	v_mfma_f32_16x16x32_f16 v[106:109], v[156:159], v[188:191], v[106:109]
	v_mfma_f32_16x16x32_f16 v[126:129], v[152:155], v[172:175], v[126:129]
	v_mfma_f32_16x16x32_f16 v[122:125], v[164:167], v[172:175], v[122:125]
	v_mfma_f32_16x16x32_f16 v[118:121], v[134:137], v[176:179], v[118:121]
	v_mfma_f32_16x16x32_f16 v[114:117], v[156:159], v[176:179], v[114:117]
	v_mfma_f32_16x16x32_f16 v[110:113], v[152:155], v[192:195], v[110:113]
	v_mfma_f32_16x16x32_f16 v[106:109], v[164:167], v[192:195], v[106:109]
	v_mfma_f32_16x16x32_f16 v[102:105], v[134:137], v[196:199], v[102:105]
	v_mfma_f32_16x16x32_f16 v[98:101], v[156:159], v[196:199], v[98:101]
	v_mfma_f32_16x16x32_f16 v[130:133], v[152:155], v[184:187], v[118:121]
	v_mfma_f32_16x16x32_f16 v[204:207], v[164:167], v[184:187], v[114:117]
	v_mfma_f32_16x16x32_f16 v[208:211], v[152:155], v[200:203], v[102:105]
	v_mfma_f32_16x16x32_f16 v[212:215], v[164:167], v[200:203], v[98:101]
	s_barrier
	s_nop 1
	ds_read_b128 v[98:101], v150
	ds_read_b128 v[102:105], v150 offset:1024
	ds_read_b128 v[114:117], v150 offset:2048
	ds_read_b128 v[118:121], v150 offset:3072
	s_barrier
	s_waitcnt lgkmcnt(0)
	v_mfma_f32_16x16x32_f16 v[94:97], v[98:101], v[168:171], v[94:97]
	v_mfma_f32_16x16x32_f16 v[90:93], v[114:117], v[168:171], v[90:93]
	v_mfma_f32_16x16x32_f16 v[78:81], v[98:101], v[188:191], v[78:81]
	v_mfma_f32_16x16x32_f16 v[74:77], v[114:117], v[188:191], v[74:77]
	v_mfma_f32_16x16x32_f16 v[94:97], v[102:105], v[172:175], v[94:97]
	v_mfma_f32_16x16x32_f16 v[90:93], v[118:121], v[172:175], v[90:93]
	v_mfma_f32_16x16x32_f16 v[86:89], v[98:101], v[176:179], v[86:89]
	v_mfma_f32_16x16x32_f16 v[82:85], v[114:117], v[176:179], v[82:85]
	v_mfma_f32_16x16x32_f16 v[78:81], v[102:105], v[192:195], v[78:81]
	v_mfma_f32_16x16x32_f16 v[74:77], v[118:121], v[192:195], v[74:77]
	v_mfma_f32_16x16x32_f16 v[70:73], v[98:101], v[196:199], v[70:73]
	v_mfma_f32_16x16x32_f16 v[66:69], v[114:117], v[196:199], v[66:69]
	v_mfma_f32_16x16x32_f16 v[168:171], v[102:105], v[184:187], v[86:89]
	v_mfma_f32_16x16x32_f16 v[172:175], v[118:121], v[184:187], v[82:85]
	v_mfma_f32_16x16x32_f16 v[176:179], v[102:105], v[200:203], v[70:73]
	v_mfma_f32_16x16x32_f16 v[184:187], v[118:121], v[200:203], v[66:69]
	s_barrier
	s_nop 1
	ds_read_b128 v[66:69], v147 offset:16384
	ds_read_b128 v[70:73], v147 offset:17408
	ds_read_b128 v[82:85], v146 offset:16384
	ds_read_b128 v[86:89], v146 offset:17408
	ds_read_b128 v[188:191], v145 offset:16384
	ds_read_b128 v[192:195], v145 offset:17408
	ds_read_b128 v[196:199], v144 offset:16384
	ds_read_b128 v[200:203], v144 offset:17408
	s_waitcnt vmcnt(4)
	s_barrier
	s_waitcnt lgkmcnt(0)
	v_mfma_f32_16x16x32_f16 v[62:65], v[134:137], v[66:69], v[62:65]
	v_mfma_f32_16x16x32_f16 v[58:61], v[156:159], v[66:69], v[58:61]
	v_mfma_f32_16x16x32_f16 v[46:49], v[134:137], v[188:191], v[46:49]
	v_mfma_f32_16x16x32_f16 v[42:45], v[156:159], v[188:191], v[42:45]
	v_mfma_f32_16x16x32_f16 v[62:65], v[152:155], v[70:73], v[62:65]
	v_mfma_f32_16x16x32_f16 v[58:61], v[164:167], v[70:73], v[58:61]
	v_mfma_f32_16x16x32_f16 v[54:57], v[134:137], v[82:85], v[54:57]
	v_mfma_f32_16x16x32_f16 v[50:53], v[156:159], v[82:85], v[50:53]
	v_mfma_f32_16x16x32_f16 v[46:49], v[152:155], v[192:195], v[46:49]
	v_mfma_f32_16x16x32_f16 v[42:45], v[164:167], v[192:195], v[42:45]
	v_mfma_f32_16x16x32_f16 v[38:41], v[134:137], v[196:199], v[38:41]
	v_mfma_f32_16x16x32_f16 v[34:37], v[156:159], v[196:199], v[34:37]
	v_mfma_f32_16x16x32_f16 v[216:219], v[152:155], v[86:89], v[54:57]
	v_mfma_f32_16x16x32_f16 v[220:223], v[164:167], v[86:89], v[50:53]
	v_mfma_f32_16x16x32_f16 v[134:137], v[152:155], v[200:203], v[38:41]
	v_mfma_f32_16x16x32_f16 v[150:153], v[164:167], v[200:203], v[34:37]
	v_mfma_f32_16x16x32_f16 v[30:33], v[98:101], v[66:69], v[30:33]
	v_mfma_f32_16x16x32_f16 v[26:29], v[114:117], v[66:69], v[26:29]
	v_mfma_f32_16x16x32_f16 v[14:17], v[98:101], v[188:191], v[14:17]
	v_mfma_f32_16x16x32_f16 v[10:13], v[114:117], v[188:191], v[10:13]
	v_mfma_f32_16x16x32_f16 v[30:33], v[102:105], v[70:73], v[30:33]
	v_mfma_f32_16x16x32_f16 v[26:29], v[118:121], v[70:73], v[26:29]
	v_mfma_f32_16x16x32_f16 v[22:25], v[98:101], v[82:85], v[22:25]
	v_mfma_f32_16x16x32_f16 v[18:21], v[114:117], v[82:85], v[18:21]
	v_mfma_f32_16x16x32_f16 v[14:17], v[102:105], v[192:195], v[14:17]
	v_mfma_f32_16x16x32_f16 v[10:13], v[118:121], v[192:195], v[10:13]
	v_mfma_f32_16x16x32_f16 v[6:9], v[98:101], v[196:199], v[6:9]
	v_mfma_f32_16x16x32_f16 v[2:5], v[114:117], v[196:199], v[2:5]
	v_mfma_f32_16x16x32_f16 v[154:157], v[102:105], v[86:89], v[22:25]
	v_mfma_f32_16x16x32_f16 v[158:161], v[118:121], v[86:89], v[18:21]
	v_mfma_f32_16x16x32_f16 v[164:167], v[102:105], v[200:203], v[6:9]
	v_mfma_f32_16x16x32_f16 v[188:191], v[118:121], v[200:203], v[2:5]
	s_barrier
	s_nop 1
	ds_read_b128 v[2:5], v149
	ds_read_b128 v[6:9], v149 offset:1024
	ds_read_b128 v[192:195], v149 offset:2048
	ds_read_b128 v[196:199], v149 offset:3072
	ds_read_b128 v[18:21], v147 offset:32768
	ds_read_b128 v[22:25], v147 offset:33792
	ds_read_b128 v[34:37], v146 offset:32768
	ds_read_b128 v[38:41], v146 offset:33792
	ds_read_b128 v[50:53], v145 offset:32768
	ds_read_b128 v[54:57], v145 offset:33792
	ds_read_b128 v[200:203], v144 offset:32768
	ds_read_b128 v[224:227], v144 offset:33792
	s_waitcnt vmcnt(2)
	s_barrier
	s_waitcnt lgkmcnt(0)
	v_mfma_f32_16x16x32_f16 v[66:69], v[2:5], v[18:21], v[126:129]
	v_mfma_f32_16x16x32_f16 v[118:121], v[6:9], v[22:25], v[66:69]
	v_mfma_f32_16x16x32_f16 v[66:69], v[192:195], v[18:21], v[122:125]
	v_mfma_f32_16x16x32_f16 v[114:117], v[196:199], v[22:25], v[66:69]
	v_mfma_f32_16x16x32_f16 v[66:69], v[2:5], v[34:37], v[130:133]
	v_mfma_f32_16x16x32_f16 v[102:105], v[6:9], v[38:41], v[66:69]
	v_mfma_f32_16x16x32_f16 v[66:69], v[192:195], v[34:37], v[204:207]
	v_mfma_f32_16x16x32_f16 v[98:101], v[196:199], v[38:41], v[66:69]
	v_mfma_f32_16x16x32_f16 v[66:69], v[2:5], v[50:53], v[110:113]
	v_mfma_f32_16x16x32_f16 v[86:89], v[6:9], v[54:57], v[66:69]
	v_mfma_f32_16x16x32_f16 v[66:69], v[192:195], v[50:53], v[106:109]
	v_mfma_f32_16x16x32_f16 v[82:85], v[196:199], v[54:57], v[66:69]
	v_mfma_f32_16x16x32_f16 v[66:69], v[2:5], v[200:203], v[208:211]
	v_mfma_f32_16x16x32_f16 v[70:73], v[6:9], v[224:227], v[66:69]
	v_mfma_f32_16x16x32_f16 v[66:69], v[192:195], v[200:203], v[212:215]
	v_mfma_f32_16x16x32_f16 v[66:69], v[196:199], v[224:227], v[66:69]
	s_barrier
	ds_read_b128 v[130:133], v148
	ds_read_b128 v[204:207], v148 offset:1024
	ds_read_b128 v[208:211], v148 offset:2048
	ds_read_b128 v[212:215], v148 offset:3072
	s_waitcnt vmcnt(0)
	s_barrier
	s_waitcnt lgkmcnt(0)
	v_mfma_f32_16x16x32_f16 v[94:97], v[130:133], v[18:21], v[94:97]
	v_mfma_f32_16x16x32_f16 v[18:21], v[208:211], v[18:21], v[90:93]
	v_mfma_f32_16x16x32_f16 v[122:125], v[212:215], v[22:25], v[18:21]
	v_mfma_f32_16x16x32_f16 v[18:21], v[130:133], v[34:37], v[168:171]
	v_mfma_f32_16x16x32_f16 v[110:113], v[204:207], v[38:41], v[18:21]
	v_mfma_f32_16x16x32_f16 v[18:21], v[208:211], v[34:37], v[172:175]
	v_mfma_f32_16x16x32_f16 v[106:109], v[212:215], v[38:41], v[18:21]
	v_mfma_f32_16x16x32_f16 v[18:21], v[130:133], v[50:53], v[78:81]
	v_mfma_f32_16x16x32_f16 v[126:129], v[204:207], v[22:25], v[94:97]
	v_mfma_f32_16x16x32_f16 v[94:97], v[204:207], v[54:57], v[18:21]
	v_mfma_f32_16x16x32_f16 v[18:21], v[208:211], v[50:53], v[74:77]
	v_mfma_f32_16x16x32_f16 v[90:93], v[212:215], v[54:57], v[18:21]
	v_mfma_f32_16x16x32_f16 v[18:21], v[130:133], v[200:203], v[176:179]
	v_mfma_f32_16x16x32_f16 v[78:81], v[204:207], v[224:227], v[18:21]
	v_mfma_f32_16x16x32_f16 v[18:21], v[208:211], v[200:203], v[184:187]
	v_mfma_f32_16x16x32_f16 v[74:77], v[212:215], v[224:227], v[18:21]
	s_barrier
	ds_read_b128 v[168:171], v147 offset:49152
	ds_read_b128 v[172:175], v147 offset:50176
	ds_read_b128 v[176:179], v146 offset:49152
	ds_read_b128 v[146:149], v146 offset:50176
	ds_read_b128 v[184:187], v145 offset:49152
	ds_read_b128 v[200:203], v145 offset:50176
	ds_read_b128 v[224:227], v144 offset:49152
	ds_read_b128 v[228:231], v144 offset:50176
	s_barrier
	s_waitcnt lgkmcnt(0)
	v_mfma_f32_16x16x32_f16 v[18:21], v[2:5], v[168:171], v[62:65]
	v_mfma_f32_16x16x32_f16 v[54:57], v[6:9], v[172:175], v[18:21]
	v_mfma_f32_16x16x32_f16 v[18:21], v[192:195], v[168:171], v[58:61]
	v_mfma_f32_16x16x32_f16 v[50:53], v[196:199], v[172:175], v[18:21]
	v_mfma_f32_16x16x32_f16 v[18:21], v[2:5], v[176:179], v[216:219]
	v_mfma_f32_16x16x32_f16 v[38:41], v[6:9], v[146:149], v[18:21]
	v_mfma_f32_16x16x32_f16 v[18:21], v[192:195], v[176:179], v[220:223]
	v_mfma_f32_16x16x32_f16 v[34:37], v[196:199], v[146:149], v[18:21]
	v_mfma_f32_16x16x32_f16 v[18:21], v[2:5], v[184:187], v[46:49]
	v_mfma_f32_16x16x32_f16 v[2:5], v[2:5], v[224:227], v[134:137]
	v_mfma_f32_16x16x32_f16 v[22:25], v[6:9], v[200:203], v[18:21]
	v_mfma_f32_16x16x32_f16 v[18:21], v[192:195], v[184:187], v[42:45]
	v_mfma_f32_16x16x32_f16 v[6:9], v[6:9], v[228:231], v[2:5]
	v_mfma_f32_16x16x32_f16 v[2:5], v[192:195], v[224:227], v[150:153]
	v_mfma_f32_16x16x32_f16 v[18:21], v[196:199], v[200:203], v[18:21]
	v_mfma_f32_16x16x32_f16 v[2:5], v[196:199], v[228:231], v[2:5]
	v_mfma_f32_16x16x32_f16 v[26:29], v[208:211], v[168:171], v[26:29]
	v_mfma_f32_16x16x32_f16 v[58:61], v[212:215], v[172:175], v[26:29]
	v_mfma_f32_16x16x32_f16 v[26:29], v[130:133], v[176:179], v[154:157]
	v_mfma_f32_16x16x32_f16 v[46:49], v[204:207], v[146:149], v[26:29]
	v_mfma_f32_16x16x32_f16 v[26:29], v[208:211], v[176:179], v[158:161]
	v_mfma_f32_16x16x32_f16 v[10:13], v[208:211], v[184:187], v[10:13]
	v_mfma_f32_16x16x32_f16 v[30:33], v[130:133], v[168:171], v[30:33]
	v_mfma_f32_16x16x32_f16 v[42:45], v[212:215], v[146:149], v[26:29]
	v_mfma_f32_16x16x32_f16 v[14:17], v[130:133], v[184:187], v[14:17]
	v_mfma_f32_16x16x32_f16 v[26:29], v[212:215], v[200:203], v[10:13]
	v_mfma_f32_16x16x32_f16 v[10:13], v[130:133], v[224:227], v[164:167]
	v_mfma_f32_16x16x32_f16 v[62:65], v[204:207], v[172:175], v[30:33]
	v_mfma_f32_16x16x32_f16 v[30:33], v[204:207], v[200:203], v[14:17]
	v_mfma_f32_16x16x32_f16 v[14:17], v[204:207], v[228:231], v[10:13]
	v_mfma_f32_16x16x32_f16 v[10:13], v[208:211], v[224:227], v[188:191]
	v_mfma_f32_16x16x32_f16 v[10:13], v[212:215], v[228:231], v[10:13]
